# P2: memory K/V projection GEMM units moved from 32 even WGs to odd (streaming) WGs with a completion counter; counted vmcnt waits in expert-weight conversion loop
# speedup vs baseline: 1.4044x; 1.4044x over previous
.LBB0_319:
	v_cmp_eq_u32_e64 s[0:1], 0, v0
	s_nop 1
	v_writelane_b32 v255, s0, 42
	s_nop 1
	v_writelane_b32 v255, s1, 43
	s_nop 0
	v_readlane_b32 s0, v255, 6
	v_readlane_b32 s1, v255, 7
	s_andn2_b64 vcc, exec, s[0:1]
	v_readlane_b32 s0, v255, 2
	s_and_b32 s0, s0, 7
	s_nop 0
	v_writelane_b32 v255, s0, 44
	s_cbranch_vccnz .LBB0_925
	s_mov_b64 s[0:1], s[90:91]
	s_andn2_b64 vcc, exec, s[62:63]
	v_writelane_b32 v255, s0, 45
	s_load_dwordx2 s[92:93], s[0:1], 0x100
	s_waitcnt lgkmcnt(0)
	v_writelane_b32 v255, s1, 46
	v_writelane_b32 v255, s94, 47
	v_writelane_b32 v255, s73, 48
	s_mov_b32 s101, 0
	s_cbranch_vccnz .Lodd_kv_entry
	v_writelane_b32 v255, s90, 28
	s_ashr_i32 s0, s78, 4
	s_and_b32 s1, s78, 14
	v_writelane_b32 v255, s91, 29
	s_ashr_i32 s2, s78, 7
	s_lshl_b32 s4, s0, 7
	v_writelane_b32 v255, s1, 49
	s_ashr_i32 s3, s2, 31
	s_ashr_i32 s5, s4, 31
	s_ashr_i32 s1, s0, 31
	s_and_b32 s8, s0, 7
	s_lshl_b64 s[6:7], s[2:3], 25
	s_lshl_b64 s[0:1], s[0:1], 15
	s_lshl_b32 s9, s2, 13
	s_lshl_b64 s[4:5], s[4:5], 2
	s_add_u32 s4, s92, s4
	s_addc_u32 s5, s93, s5
	s_add_u32 s4, s4, 0x7c00
	s_addc_u32 s5, s5, 0
	s_lshl_b64 s[84:85], s[2:3], 24
	s_lshl_b32 s2, s8, 8
	v_writelane_b32 v255, s9, 32
	s_or_b32 s84, s84, s2
	v_writelane_b32 v255, s4, 50
	s_add_u32 s3, s92, s84
	s_mov_b32 s72, 0xfffc0000
	v_writelane_b32 v255, s5, 51
	s_addc_u32 s4, s93, s85
	s_add_u32 s10, s3, 0xe000000
	s_addc_u32 s11, s4, 0
	s_add_u32 s88, s3, 0x10000000
	v_writelane_b32 v255, s10, 4
	s_addc_u32 s89, s4, 0
	v_mbcnt_lo_u32_b32 v1, -1, 0
	v_writelane_b32 v255, s11, 5
	s_add_u32 s10, s3, 0x12000000
	s_addc_u32 s11, s4, 0
	s_add_u32 s3, s92, s6
	s_addc_u32 s4, s93, s7
	s_add_u32 s2, s3, s2
	v_writelane_b32 v255, s10, 34
	s_addc_u32 s3, s4, 0
	s_add_u32 s2, s2, 0x16000000
	v_writelane_b32 v255, s11, 35
	v_writelane_b32 v255, s2, 17
	s_addc_u32 s2, s3, 0
	v_writelane_b32 v255, s2, 26
	s_lshl_b32 s2, s8, 2
	s_add_u32 s2, s92, s2
	s_addc_u32 s3, s93, 0
	s_add_u32 s82, s2, 0x6730000
	s_addc_u32 s83, s3, 0
	s_add_u32 s0, s92, s0
	s_addc_u32 s1, s93, s1
	s_add_u32 s0, s0, 0x5db0000
	s_addc_u32 s1, s1, 0
	v_writelane_b32 v255, s0, 52
	s_mov_b32 s87, 0
	s_mov_b64 s[70:71], -1
	v_writelane_b32 v255, s1, 53
	s_mov_b32 s0, s78
	v_writelane_b32 v255, s0, 30
	v_mov_b32_e32 v197, 0
	s_mov_b32 s3, 0x41000000
	v_writelane_b32 v255, s1, 31
	s_bfe_u32 s0, s78, 0x30001
	s_lshl_b32 s1, s0, 9
	s_lshl_b32 s0, s0, 11
	s_or_b32 s2, s1, 0x7f
	s_add_i32 s0, s0, 0
	v_writelane_b32 v255, s2, 54
	s_add_i32 s0, s0, 0x10cfc
	v_writelane_b32 v255, s0, 55
	s_or_b32 s0, s1, 0x60
	v_writelane_b32 v255, s0, 56
	s_or_b32 s0, s1, 64
	v_writelane_b32 v255, s0, 57
	v_writelane_b32 v255, s1, 58
	s_or_b32 s0, s1, 32
	v_writelane_b32 v255, s0, 59
	s_mov_b32 s80, 0x3e0293ee
	s_mov_b32 s2, 0x12000000
	s_brev_b32 s33, 8
	s_mov_b32 s75, 0xc1900000
	s_add_i32 s81, 0, 0x18c04
	s_add_i32 s78, 0, 0x18c08
	s_add_i32 s79, 0, 0x18c0c
	s_add_i32 s90, 0, 0x18c10
	s_add_i32 s91, 0, 0x18c14
	s_add_i32 s96, 0, 0x18c18
	s_add_i32 s97, 0, 0x18c1c
	s_mov_b32 s73, -1
	v_mbcnt_hi_u32_b32 v1, -1, v1
	v_mov_b32_e32 v211, 0xff800000
	v_mov_b32_e32 v212, 0xf149f2ca
	s_branch .LBB0_323

.Lodd_kv_done:
	s_bfe_u32 s0, s78, 0x30001
	s_cmp_lt_u32 s0, 2
	s_cbranch_scc0 .LBB0_886
	v_cmp_eq_u32_e32 vcc, 0, v0
	s_and_saveexec_b64 s[0:1], vcc
	s_cbranch_execz .Lodd_kv_sig_skip
	buffer_wbl2 sc1
	s_waitcnt vmcnt(0)
	v_mov_b32_e32 v2, 0xf300
	v_mov_b32_e32 v3, 1
	global_atomic_add v2, v3, s[92:93]
	s_waitcnt vmcnt(0)
.Lodd_kv_sig_skip:
	s_or_b64 exec, exec, s[0:1]
	s_branch .LBB0_886
.Lodd_kv_entry:
	s_ashr_i32 s2, s78, 1
	s_mov_b32 s101, 1
.LBB0_770:
	s_and_b32 s0, s2, 7
	v_readlane_b32 s2, v255, 36
	s_and_b32 s1, s2, -2
	s_or_b32 s1, s1, s0
	s_cmp_lt_u32 s0, 2
	s_cselect_b32 s2, s1, 0x100000
	s_cmp_eq_u32 s101, 0
	s_cselect_b32 s2, 0x100000, s2
	v_mov_b32_e32 v10, v0
	s_cmp_gt_i32 s2, 31
	v_readlane_b32 s3, v255, 37
	v_readfirstlane_b32 s1, v10
	s_cbranch_scc1 .LBB0_790
	v_lshlrev_b32_e32 v2, 4, v10
	v_add_u32_e32 v3, 0x2000, v2
	v_ashrrev_i32_e32 v4, 31, v3
	v_lshrrev_b32_e32 v4, 22, v4
	v_add_u32_e32 v4, v3, v4
	v_ashrrev_i32_e32 v4, 10, v4
	v_mul_i32_i24_e32 v5, 0x400, v4
	v_sub_u32_e32 v3, v3, v5
	v_lshrrev_b32_e32 v5, 4, v3
	v_bitop3_b32 v3, v5, v3, 32 bitop3:0x6c
	v_ashrrev_i32_e32 v5, 31, v3
	v_lshrrev_b32_e32 v5, 26, v5
	s_add_u32 s3, s92, 0x6130000
	v_add_u32_e32 v5, v3, v5
	s_addc_u32 s33, s93, 0
	v_ashrrev_i32_e32 v6, 6, v5
	v_and_b32_e32 v5, 0xc0, v5
	s_add_u32 s40, s92, 0x2300000
	v_sub_u32_e32 v3, v3, v5
	v_mov_b32_e32 v5, 1
	s_addc_u32 s41, s93, 0
	s_ashr_i32 s43, s2, 31
	v_lshlrev_b32_e32 v7, 3, v4
	v_lshlrev_b32_e32 v4, 5, v4
	v_ashrrev_i16_sdwa v3, v5, sext(v3) dst_sel:DWORD dst_unused:UNUSED_PAD src0_sel:DWORD src1_sel:BYTE_0
	s_lshr_b32 s0, s43, 29
	v_and_b32_e32 v7, -16, v7
	v_and_b32_e32 v4, 32, v4
	v_bfe_i32 v3, v3, 0, 16
	s_add_i32 s0, s2, s0
	v_add_u32_e32 v7, v6, v7
	v_add_lshl_u32 v3, v4, v3, 1
	v_bfe_i32 v4, v10, 27, 1
	s_ashr_i32 s4, s0, 3
	s_and_b32 s0, s0, -8
	v_and_b32_e32 v6, 3, v6
	s_mov_b32 s6, 0xfffe0
	v_lshrrev_b32_e32 v8, 2, v7
	v_lshlrev_b32_e32 v9, 1, v7
	v_lshrrev_b32_e32 v4, 22, v4
	s_ashr_i32 s8, s1, 6
	s_sub_i32 s0, s2, s0
	v_and_or_b32 v6, v7, s6, v6
	v_and_b32_e32 v8, 4, v8
	v_and_b32_e32 v9, 24, v9
	v_add_u32_e32 v4, v2, v4
	s_ashr_i32 s10, s1, 8
	s_lshl_b32 s42, s8, 10
	s_lshl_b32 s5, s0, 2
	v_or3_b32 v6, v6, v8, v9
	v_and_b32_e32 v4, 0xfffffc00, v4
	s_cmp_lt_i32 s0, 0
	s_mul_i32 s0, s0, 5
	v_lshl_add_u32 v130, v6, 12, v3
	v_sub_u32_e32 v2, v2, v4
	v_ashrrev_i32_e32 v6, 31, v10
	v_lshrrev_b32_e32 v4, 4, v2
	v_lshrrev_b32_e32 v6, 26, v6
	s_cselect_b32 s0, s0, s5
	v_bitop3_b32 v4, v4, v2, 32 bitop3:0x6c
	v_ashrrev_i32_e32 v2, 31, v2
	v_add_u32_e32 v6, v10, v6
	s_add_i32 s0, s0, s4
	v_lshrrev_b32_e32 v2, 26, v2
	v_ashrrev_i32_e32 v6, 6, v6
	s_ashr_i32 s4, s0, 31
	v_add_u32_e32 v2, v4, v2
	v_lshlrev_b32_e32 v8, 3, v6
	s_lshr_b32 s4, s4, 25
	v_ashrrev_i32_e32 v2, 6, v2
	v_and_b32_e32 v8, -16, v8
	s_add_i32 s4, s0, s4
	v_add_u32_e32 v8, v2, v8
	v_and_b32_e32 v9, 3, v2
	s_ashr_i32 s5, s4, 7
	v_and_or_b32 v9, v8, s6, v9
	v_mul_i32_i24_e32 v2, 64, v2
	s_lshl_b32 s6, s5, 3
	v_sub_u32_e32 v2, v4, v2
	s_sub_i32 s5, 2, s6
	v_lshlrev_b32_e32 v6, 5, v6
	v_ashrrev_i16_sdwa v2, v5, sext(v2) dst_sel:DWORD dst_unused:UNUSED_PAD src0_sel:DWORD src1_sel:BYTE_0
	s_min_u32 s7, s5, 8
	s_and_b32 s4, s4, 0xffffff80
	v_and_b32_e32 v6, 32, v6
	v_bfe_i32 v2, v2, 0, 16
	s_sub_i32 s9, s0, s4
	v_cvt_f32_ubyte0_e32 v5, s7
	v_add_lshl_u32 v2, v6, v2, 1
	v_cvt_f32_i32_e32 v4, s9
	v_rcp_iflag_f32_e32 v6, v5
	s_ashr_i32 s0, s9, 30
	s_or_b32 s0, s0, 1
	v_lshrrev_b32_e32 v11, 2, v8
	v_mul_f32_e32 v6, v4, v6
	v_trunc_f32_e32 v6, v6
	v_fma_f32 v4, -v6, v5, v4
	v_cvt_i32_f32_e32 v6, v6
	v_cmp_ge_f32_e64 s[4:5], |v4|, v5
	s_and_b64 s[4:5], s[4:5], exec
	s_cselect_b32 s0, s0, 0
	v_readfirstlane_b32 s4, v6
	s_add_i32 s0, s4, s0
	s_mul_i32 s4, s0, s7
	s_sub_i32 s4, s9, s4
	s_sext_i32_i8 s4, s4
	s_add_i32 s22, s6, s4
	s_ashr_i32 s23, s22, 31
	s_bfe_i64 s[6:7], s[0:1], 0x80000
	s_lshl_b64 s[4:5], s[22:23], 20
	s_lshl_b64 s[6:7], s[6:7], 20
	s_add_u32 s28, s3, s4
	v_lshlrev_b32_e32 v12, 1, v8
	s_addc_u32 s29, s33, s5
	v_and_b32_e32 v11, 4, v11
	v_and_b32_e32 v12, 24, v12
	s_add_u32 s30, s40, s6
	v_or3_b32 v9, v9, v11, v12
	s_addc_u32 s31, s41, s7
	s_add_i32 s23, s42, 0
	v_lshl_add_u32 v132, v9, 12, v2
	s_add_i32 m0, s23, 0x10000
	v_lshl_add_u32 v134, v8, 12, v2
	global_load_lds_dwordx4 v132, s[30:31]
	s_add_i32 m0, s23, 0x12000
	s_add_u32 s4, s30, 0x80000
	global_load_lds_dwordx4 v130, s[30:31]
	s_addc_u32 s5, s31, 0
	s_add_i32 m0, s23, 0x14000
	s_add_i32 s44, s23, 0x2000
	global_load_lds_dwordx4 v132, s[4:5]
	s_add_i32 m0, s23, 0x16000
	v_lshl_add_u32 v136, v7, 12, v3
	global_load_lds_dwordx4 v130, s[4:5]
	s_mov_b32 m0, s23
	s_add_i32 s45, s23, 0x4000
	global_load_lds_dwordx4 v134, s[28:29]
	s_mov_b32 m0, s44
	v_add_u32_e32 v138, 0x80000, v134
	global_load_lds_dwordx4 v136, s[28:29]
	s_mov_b32 m0, s45
	s_add_i32 s46, s23, 0x6000
	v_add_u32_e32 v140, 0x80000, v136
	global_load_lds_dwordx4 v138, s[28:29]
	s_mov_b32 m0, s46
	v_mov_b32_e32 v133, 0
	global_load_lds_dwordx4 v140, s[28:29]
	v_mov_b32_e32 v131, v133
	v_mov_b32_e32 v135, v133
	v_mov_b32_e32 v137, v133
	s_cmp_eq_u32 s10, 1
	s_mov_b32 s47, 0
	v_lshl_add_u64 v[8:9], s[30:31], 0, v[132:133]
	v_lshl_add_u64 v[6:7], s[30:31], 0, v[130:131]
	v_lshl_add_u64 v[2:3], s[28:29], 0, v[134:135]
	s_cselect_b64 s[4:5], -1, 0
	s_cmp_lg_u32 s10, 1
	v_lshl_add_u64 v[4:5], s[28:29], 0, v[136:137]
	s_cbranch_scc1 .LBB0_773
	s_barrier

.LBB0_790:
	s_cmp_eq_u32 s101, 1
	s_cbranch_scc1 .Lodd_kv_done
	v_readlane_b32 s0, v255, 8
	v_readlane_b32 s1, v255, 9
	s_and_b64 vcc, exec, s[0:1]
	s_cbranch_vccz .LBB0_886
	s_mov_b32 s1, 0
.Lkv_poll:
	v_mov_b32_e32 v2, 0xf300
	global_load_dword v2, v2, s[92:93] sc1
	s_waitcnt vmcnt(0)
	v_readfirstlane_b32 s0, v2
	s_cmp_ge_u32 s0, 32
	s_cbranch_scc1 .Lkv_ready
	s_add_i32 s1, s1, 1
	s_cmp_gt_u32 s1, 0xffff
	s_cbranch_scc1 .Lkv_ready
	s_sleep 1
	s_branch .Lkv_poll
.Lkv_ready:
	s_waitcnt vmcnt(0)
	s_waitcnt vmcnt(0)
	s_barrier
	s_mov_b64 s[4:5], exec
	v_readlane_b32 s0, v255, 42
	v_readlane_b32 s1, v255, 43
	v_readlane_b32 s24, v255, 45
	s_and_b64 s[0:1], s[4:5], s[0:1]
	v_readlane_b32 s25, v255, 46
	s_mov_b64 exec, s[0:1]
	s_cbranch_execz .LBB0_836
	v_readlane_b32 s0, v255, 14
	s_waitcnt vmcnt(0) expcnt(0) lgkmcnt(0)
	s_nop 0
	v_mov_b32_e32 v2, s0
	ds_read_b32 v4, v2
	ds_read_b32 v2, v2 offset:4
	v_readlane_b32 s0, v255, 10
	v_readlane_b32 s1, v255, 11
	s_add_u32 s6, s0, 0x200
	s_waitcnt lgkmcnt(1)
	v_cmp_ne_u32_e32 vcc, 0, v4
	s_addc_u32 s7, s1, 0
	s_cbranch_vccnz .LBB0_807
	v_readlane_b32 s0, v255, 3
	s_cmp_lg_u32 s0, 0
	s_cbranch_scc1 .LBB0_795
	v_readlane_b32 s2, v255, 0
	v_readlane_b32 s3, v255, 1
	s_load_dwordx2 s[0:1], s[2:3], 0x4
	v_readlane_b32 s2, v255, 19
	s_waitcnt lgkmcnt(0)
	s_mul_i32 s0, s0, s2
	s_mul_i32 s0, s0, s1
	v_writelane_b32 v255, s0, 3

.LBB0_901:
	s_or_b64 exec, exec, s[0:1]
	v_mov_b32_e32 v142, s18
	s_waitcnt lgkmcnt(0)
	s_barrier
	ds_read_b32 v142, v142
	s_waitcnt lgkmcnt(0)
	v_readfirstlane_b32 s42, v142
	s_add_i32 s42, s42, s2
	s_cmp_gt_i32 s42, 0x17fff
	s_cbranch_scc1 .LBB0_906
	s_cmp_gt_i32 s42, 0xffff
	s_mov_b64 s[0:1], -1
	s_cbranch_scc0 .LBB0_904
	s_load_dwordx2 s[0:1], s[46:47], 0xe0
	s_add_i32 s8, s42, 0xffff0000
	s_lshr_b32 s8, s8, 10
	s_lshl_b64 s[12:13], s[8:9], 24
	v_mov_b32_e32 v45, v131
	s_waitcnt lgkmcnt(0)
	s_add_u32 s0, s0, s12
	s_addc_u32 s1, s1, s13
	s_lshl_b32 s8, s42, 1
	s_and_b32 s8, s8, 0x780
	v_or_b32_e32 v44, s8, v1
	s_lshl_b32 s8, s42, 7
	s_and_b32 s8, s8, 0x1f80
	s_add_u32 s0, s0, s8
	s_addc_u32 s1, s1, 0
	v_lshl_add_u64 v[42:43], s[0:1], 0, v[130:131]
	v_lshlrev_b32_e32 v44, 13, v44
	v_lshl_add_u64 v[122:123], v[42:43], 0, v[44:45]
	v_add_co_u32_e32 v46, vcc, s19, v122
	s_mov_b64 s[0:1], 0
	s_nop 0
	v_addc_co_u32_e32 v47, vcc, 0, v123, vcc
	v_add_co_u32_e32 v58, vcc, s20, v122
	global_load_dwordx4 v[42:45], v[122:123], off nt
	s_nop 0
	global_load_dwordx4 v[46:49], v[46:47], off nt
	v_addc_co_u32_e32 v59, vcc, 0, v123, vcc
	v_add_co_u32_e32 v62, vcc, s21, v122
	s_nop 1
	v_addc_co_u32_e32 v63, vcc, 0, v123, vcc
	v_add_co_u32_e32 v70, vcc, s23, v122
	global_load_dwordx4 v[58:61], v[58:59], off nt
	s_nop 0
	global_load_dwordx4 v[62:65], v[62:63], off nt
	v_addc_co_u32_e32 v71, vcc, 0, v123, vcc
	v_add_co_u32_e32 v78, vcc, s24, v122
	s_nop 1
	v_addc_co_u32_e32 v79, vcc, 0, v123, vcc
	v_add_co_u32_e32 v82, vcc, s25, v122
	global_load_dwordx4 v[70:73], v[70:71], off nt
	s_nop 0
	global_load_dwordx4 v[78:81], v[78:79], off nt
	v_addc_co_u32_e32 v83, vcc, 0, v123, vcc
	v_add_co_u32_e32 v90, vcc, s26, v122
	s_nop 1
	v_addc_co_u32_e32 v91, vcc, 0, v123, vcc
	v_add_co_u32_e32 v98, vcc, s27, v122
	global_load_dwordx4 v[82:85], v[82:83], off nt
	s_nop 0
	global_load_dwordx4 v[90:93], v[90:91], off nt
	v_addc_co_u32_e32 v99, vcc, 0, v123, vcc
	v_add_co_u32_e32 v102, vcc, s28, v122
	s_nop 1
	v_addc_co_u32_e32 v103, vcc, 0, v123, vcc
	v_add_co_u32_e32 v106, vcc, s29, v122
	global_load_dwordx4 v[98:101], v[98:99], off nt
	s_nop 0
	global_load_dwordx4 v[102:105], v[102:103], off nt
	v_addc_co_u32_e32 v107, vcc, 0, v123, vcc
	v_add_co_u32_e32 v110, vcc, s30, v122
	s_nop 1
	v_addc_co_u32_e32 v111, vcc, 0, v123, vcc
	v_add_co_u32_e32 v114, vcc, s31, v122
	global_load_dwordx4 v[106:109], v[106:107], off nt
	s_nop 0
	global_load_dwordx4 v[110:113], v[110:111], off nt
	v_addc_co_u32_e32 v115, vcc, 0, v123, vcc
	v_add_co_u32_e32 v118, vcc, 0xd0000, v122
	s_nop 1
	v_addc_co_u32_e32 v119, vcc, 0, v123, vcc
	v_add_co_u32_e32 v124, vcc, 0xe0000, v122
	global_load_dwordx4 v[114:117], v[114:115], off nt
	s_nop 0
	global_load_dwordx4 v[118:121], v[118:119], off nt
	v_addc_co_u32_e32 v125, vcc, 0, v123, vcc
	v_add_co_u32_e32 v126, vcc, 0xf0000, v122
	s_nop 1
	v_addc_co_u32_e32 v127, vcc, 0, v123, vcc
	global_load_dwordx4 v[122:125], v[124:125], off nt
	s_nop 0
	global_load_dwordx4 v[126:129], v[126:127], off nt
.LBB0_904:
	s_andn2_b64 vcc, exec, s[0:1]
	s_cbranch_vccnz .LBB0_906
	s_ashr_i32 s0, s42, 31
	s_lshr_b32 s0, s0, 21
	s_add_i32 s8, s42, s0
	s_load_dwordx2 s[0:1], s[46:47], 0xd0
	s_and_b32 s12, s8, 0xf800
	s_sub_i32 s14, s42, s12
	s_ashr_i32 s12, s8, 11
	s_ashr_i32 s13, s12, 31
	s_lshl_b64 s[12:13], s[12:13], 25
	s_waitcnt lgkmcnt(0)
	s_add_u32 s8, s0, s12
	s_sext_i32_i16 s0, s14
	s_addc_u32 s12, s1, s13
	s_bfe_u32 s0, s0, 0x70018
	s_add_i32 s0, s14, s0
	s_sext_i32_i16 s1, s0
	s_and_b32 s0, s0, 0xff80
	s_sub_i32 s0, s14, s0
	s_sext_i32_i16 s0, s0
	s_and_b32 s1, s1, 0xffffff80
	s_lshl_b32 s0, s0, 5
	v_or_b32_e32 v122, s1, v1
	s_ashr_i32 s1, s0, 31
	s_lshl_b64 s[0:1], s[0:1], 2
	v_ashrrev_i32_e32 v123, 31, v122
	s_add_u32 s0, s8, s0
	v_lshlrev_b64 v[42:43], 14, v[122:123]
	v_or_b32_e32 v44, 8, v122
	v_or_b32_e32 v58, 16, v122
	v_or_b32_e32 v60, 24, v122
	v_or_b32_e32 v70, 32, v122
	v_or_b32_e32 v72, 40, v122
	v_or_b32_e32 v82, 48, v122
	v_or_b32_e32 v84, 56, v122
	v_or_b32_e32 v98, 64, v122
	v_or_b32_e32 v100, 0x48, v122
	v_or_b32_e32 v106, 0x50, v122
	v_or_b32_e32 v108, 0x58, v122
	v_or_b32_e32 v114, 0x60, v122
	v_or_b32_e32 v116, 0x68, v122
	v_or_b32_e32 v126, 0x70, v122
	v_or_b32_e32 v122, 0x78, v122
	s_addc_u32 s1, s12, s1
	v_ashrrev_i32_e32 v45, 31, v44
	v_ashrrev_i32_e32 v59, 31, v58
	v_ashrrev_i32_e32 v61, 31, v60
	v_ashrrev_i32_e32 v71, 31, v70
	v_ashrrev_i32_e32 v73, 31, v72
	v_ashrrev_i32_e32 v83, 31, v82
	v_ashrrev_i32_e32 v85, 31, v84
	v_ashrrev_i32_e32 v99, 31, v98
	v_ashrrev_i32_e32 v101, 31, v100
	v_ashrrev_i32_e32 v107, 31, v106
	v_ashrrev_i32_e32 v109, 31, v108
	v_ashrrev_i32_e32 v115, 31, v114
	v_ashrrev_i32_e32 v117, 31, v116
	v_ashrrev_i32_e32 v127, 31, v126
	v_ashrrev_i32_e32 v123, 31, v122
	v_lshl_add_u64 v[124:125], s[0:1], 0, v[130:131]
	v_lshlrev_b64 v[44:45], 14, v[44:45]
	v_lshlrev_b64 v[58:59], 14, v[58:59]
	v_lshlrev_b64 v[60:61], 14, v[60:61]
	v_lshlrev_b64 v[70:71], 14, v[70:71]
	v_lshlrev_b64 v[72:73], 14, v[72:73]
	v_lshlrev_b64 v[82:83], 14, v[82:83]
	v_lshlrev_b64 v[84:85], 14, v[84:85]
	v_lshlrev_b64 v[98:99], 14, v[98:99]
	v_lshlrev_b64 v[100:101], 14, v[100:101]
	v_lshlrev_b64 v[106:107], 14, v[106:107]
	v_lshlrev_b64 v[108:109], 14, v[108:109]
	v_lshlrev_b64 v[114:115], 14, v[114:115]
	v_lshlrev_b64 v[116:117], 14, v[116:117]
	v_lshlrev_b64 v[126:127], 14, v[126:127]
	v_lshlrev_b64 v[122:123], 14, v[122:123]
	v_lshl_add_u64 v[42:43], v[124:125], 0, v[42:43]
	v_lshl_add_u64 v[46:47], v[124:125], 0, v[44:45]
	v_lshl_add_u64 v[58:59], v[124:125], 0, v[58:59]
	v_lshl_add_u64 v[62:63], v[124:125], 0, v[60:61]
	v_lshl_add_u64 v[70:71], v[124:125], 0, v[70:71]
	v_lshl_add_u64 v[78:79], v[124:125], 0, v[72:73]
	v_lshl_add_u64 v[82:83], v[124:125], 0, v[82:83]
	v_lshl_add_u64 v[90:91], v[124:125], 0, v[84:85]
	v_lshl_add_u64 v[98:99], v[124:125], 0, v[98:99]
	v_lshl_add_u64 v[102:103], v[124:125], 0, v[100:101]
	v_lshl_add_u64 v[106:107], v[124:125], 0, v[106:107]
	v_lshl_add_u64 v[110:111], v[124:125], 0, v[108:109]
	v_lshl_add_u64 v[114:115], v[124:125], 0, v[114:115]
	v_lshl_add_u64 v[118:119], v[124:125], 0, v[116:117]
	v_lshl_add_u64 v[126:127], v[124:125], 0, v[126:127]
	v_lshl_add_u64 v[128:129], v[124:125], 0, v[122:123]
	global_load_dwordx4 v[42:45], v[42:43], off nt
	s_nop 0
	global_load_dwordx4 v[46:49], v[46:47], off nt
	s_nop 0
	global_load_dwordx4 v[58:61], v[58:59], off nt
	s_nop 0
	global_load_dwordx4 v[62:65], v[62:63], off nt
	s_nop 0
	global_load_dwordx4 v[70:73], v[70:71], off nt
	s_nop 0
	global_load_dwordx4 v[78:81], v[78:79], off nt
	s_nop 0
	global_load_dwordx4 v[82:85], v[82:83], off nt
	s_nop 0
	global_load_dwordx4 v[90:93], v[90:91], off nt
	s_nop 0
	global_load_dwordx4 v[98:101], v[98:99], off nt
	s_nop 0
	global_load_dwordx4 v[102:105], v[102:103], off nt
	s_nop 0
	global_load_dwordx4 v[106:109], v[106:107], off nt
	s_nop 0
	global_load_dwordx4 v[110:113], v[110:111], off nt
	s_nop 0
	global_load_dwordx4 v[114:117], v[114:115], off nt
	s_nop 0
	global_load_dwordx4 v[118:121], v[118:119], off nt
	s_nop 0
	global_load_dwordx4 v[122:125], v[126:127], off nt
	s_nop 0
	global_load_dwordx4 v[126:129], v[128:129], off nt
.LBB0_906:
	s_mov_b64 s[0:1], -1
	s_cmp_gt_i32 s22, 0xffff
	v_add_u32_e32 v146, 0x400, v136
	v_add_u32_e32 v142, 0x800, v136
	v_add_u32_e32 v143, 0xa00, v136
	v_add_u32_e32 v144, 0xc00, v136
	v_add_u32_e32 v145, 0xe00, v136
	s_cbranch_scc0 .LBB0_909
	s_cmp_gt_i32 s42, 0x17fff
	s_cbranch_scc1 .Lcvw_a1_drain
	s_waitcnt vmcnt(16)
	s_branch .Lcvw_a1_go

.Lcvw_a1_go:
	v_pk_mul_f32 v[148:149], v[6:7], s[10:11] op_sel_hi:[1,0]
	v_mov_b32_e32 v147, v131
	v_cvt_pk_fp8_f32 v147, v148, v149
	v_pk_mul_f32 v[148:149], v[2:3], s[10:11] op_sel_hi:[1,0]
	v_mov_b32_e32 v150, v131
	v_cvt_pk_fp8_f32 v150, v148, v149
	v_pk_mul_f32 v[148:149], v[8:9], s[10:11] op_sel_hi:[1,0]
	v_mov_b32_e32 v151, v131
	v_cvt_pk_fp8_f32 v147, v148, v149 op_sel:[0,0,1]
	v_pk_mul_f32 v[148:149], v[4:5], s[10:11] op_sel_hi:[1,0]
	v_mov_b32_e32 v152, v131
	v_cvt_pk_fp8_f32 v150, v148, v149 op_sel:[0,0,1]
	v_pk_mul_f32 v[148:149], v[10:11], s[10:11] op_sel_hi:[1,0]
	v_mov_b32_e32 v153, v131
	v_cvt_pk_fp8_f32 v151, v148, v149
	v_pk_mul_f32 v[148:149], v[14:15], s[10:11] op_sel_hi:[1,0]
	v_mov_b32_e32 v154, v131
	v_cvt_pk_fp8_f32 v152, v148, v149
	v_pk_mul_f32 v[148:149], v[12:13], s[10:11] op_sel_hi:[1,0]
	v_mov_b32_e32 v155, v131
	v_cvt_pk_fp8_f32 v151, v148, v149 op_sel:[0,0,1]
	v_pk_mul_f32 v[148:149], v[16:17], s[10:11] op_sel_hi:[1,0]
	v_mov_b32_e32 v156, v131
	v_cvt_pk_fp8_f32 v152, v148, v149 op_sel:[0,0,1]
	v_pk_mul_f32 v[148:149], v[18:19], s[10:11] op_sel_hi:[1,0]
	s_add_i32 s0, s22, 0xffff0000
	v_cvt_pk_fp8_f32 v153, v148, v149
	v_pk_mul_f32 v[148:149], v[22:23], s[10:11] op_sel_hi:[1,0]
	s_lshr_b32 s8, s0, 10
	v_cvt_pk_fp8_f32 v154, v148, v149
	v_pk_mul_f32 v[148:149], v[20:21], s[10:11] op_sel_hi:[1,0]
	s_lshl_b32 s0, s22, 1
	v_cvt_pk_fp8_f32 v153, v148, v149 op_sel:[0,0,1]
	v_pk_mul_f32 v[148:149], v[24:25], s[10:11] op_sel_hi:[1,0]
	s_lshl_b32 s1, s22, 16
	v_cvt_pk_fp8_f32 v154, v148, v149 op_sel:[0,0,1]
	v_pk_mul_f32 v[148:149], v[26:27], s[10:11] op_sel_hi:[1,0]
	s_and_b32 s0, s0, 0x780
	v_cvt_pk_fp8_f32 v155, v148, v149
	v_pk_mul_f32 v[148:149], v[30:31], s[10:11] op_sel_hi:[1,0]
	s_and_b32 s1, s1, 0x3f0000
	v_cvt_pk_fp8_f32 v156, v148, v149
	v_pk_mul_f32 v[148:149], v[28:29], s[10:11] op_sel_hi:[1,0]
	s_lshl_b64 s[12:13], s[8:9], 22
	v_cvt_pk_fp8_f32 v155, v148, v149 op_sel:[0,0,1]
	v_pk_mul_f32 v[148:149], v[32:33], s[10:11] op_sel_hi:[1,0]
	s_add_u32 s8, s3, s12
	v_cvt_pk_fp8_f32 v156, v148, v149 op_sel:[0,0,1]
	ds_write2_b32 v136, v147, v150 offset1:72
	ds_write2_b32 v136, v151, v152 offset0:144 offset1:216
	ds_write2_b32 v146, v153, v154 offset0:32 offset1:104
	ds_write2_b32 v146, v155, v156 offset0:176 offset1:248
	v_pk_mul_f32 v[148:149], v[34:35], s[10:11] op_sel_hi:[1,0]
	v_mov_b32_e32 v147, v131
	v_cvt_pk_fp8_f32 v147, v148, v149
	v_pk_mul_f32 v[148:149], v[38:39], s[10:11] op_sel_hi:[1,0]
	v_mov_b32_e32 v150, v131
	v_cvt_pk_fp8_f32 v150, v148, v149
	v_pk_mul_f32 v[148:149], v[36:37], s[10:11] op_sel_hi:[1,0]
	v_mov_b32_e32 v151, v131
	v_cvt_pk_fp8_f32 v147, v148, v149 op_sel:[0,0,1]
	v_pk_mul_f32 v[148:149], v[40:41], s[10:11] op_sel_hi:[1,0]
	v_mov_b32_e32 v152, v131
	v_cvt_pk_fp8_f32 v150, v148, v149 op_sel:[0,0,1]
	v_pk_mul_f32 v[148:149], v[50:51], s[10:11] op_sel_hi:[1,0]
	v_mov_b32_e32 v153, v131
	v_cvt_pk_fp8_f32 v151, v148, v149
	v_pk_mul_f32 v[148:149], v[54:55], s[10:11] op_sel_hi:[1,0]
	v_mov_b32_e32 v154, v131
	v_cvt_pk_fp8_f32 v152, v148, v149
	v_pk_mul_f32 v[148:149], v[52:53], s[10:11] op_sel_hi:[1,0]
	v_mov_b32_e32 v155, v131
	v_cvt_pk_fp8_f32 v151, v148, v149 op_sel:[0,0,1]
	v_pk_mul_f32 v[148:149], v[56:57], s[10:11] op_sel_hi:[1,0]
	v_mov_b32_e32 v156, v131
	v_cvt_pk_fp8_f32 v152, v148, v149 op_sel:[0,0,1]
	v_pk_mul_f32 v[148:149], v[66:67], s[10:11] op_sel_hi:[1,0]
	s_addc_u32 s12, s11, s13
	v_cvt_pk_fp8_f32 v153, v148, v149
	v_pk_mul_f32 v[148:149], v[74:75], s[10:11] op_sel_hi:[1,0]
	s_add_u32 s0, s8, s0
	v_cvt_pk_fp8_f32 v154, v148, v149
	v_pk_mul_f32 v[148:149], v[68:69], s[10:11] op_sel_hi:[1,0]
	s_nop 0
	v_cvt_pk_fp8_f32 v153, v148, v149 op_sel:[0,0,1]
	v_pk_mul_f32 v[148:149], v[76:77], s[10:11] op_sel_hi:[1,0]
	s_nop 0
	v_cvt_pk_fp8_f32 v154, v148, v149 op_sel:[0,0,1]
	v_pk_mul_f32 v[148:149], v[86:87], s[10:11] op_sel_hi:[1,0]
	s_nop 0
	v_cvt_pk_fp8_f32 v155, v148, v149
	v_pk_mul_f32 v[148:149], v[94:95], s[10:11] op_sel_hi:[1,0]
	s_nop 0
	v_cvt_pk_fp8_f32 v156, v148, v149
	v_pk_mul_f32 v[148:149], v[88:89], s[10:11] op_sel_hi:[1,0]
	s_nop 0
	v_cvt_pk_fp8_f32 v155, v148, v149 op_sel:[0,0,1]
	v_pk_mul_f32 v[148:149], v[96:97], s[10:11] op_sel_hi:[1,0]
	s_nop 0
	v_cvt_pk_fp8_f32 v156, v148, v149 op_sel:[0,0,1]
	ds_write2_b32 v142, v147, v150 offset0:64 offset1:136
	ds_write2_b32 v143, v151, v152 offset0:80 offset1:152
	ds_write2_b32 v144, v153, v154 offset0:96 offset1:168
	ds_write2_b32 v145, v155, v156 offset0:112 offset1:184
	s_waitcnt lgkmcnt(0)
	ds_read2_b32 v[150:151], v137 offset0:18 offset1:27
	ds_read2_b32 v[148:149], v137 offset1:9
	ds_read2_b32 v[154:155], v137 offset0:54 offset1:63
	ds_read2_b32 v[164:165], v137 offset0:108 offset1:117
	ds_read2_b32 v[166:167], v137 offset0:126 offset1:135
	s_waitcnt lgkmcnt(4)
	v_perm_b32 v152, v151, v150, s33
	v_perm_b32 v153, v151, v150, s34
	ds_read2_b32 v[150:151], v137 offset0:36 offset1:45
	s_waitcnt lgkmcnt(4)
	v_perm_b32 v147, v149, v148, s33
	v_perm_b32 v149, v149, v148, s34
	v_perm_b32 v148, v152, v147, s35
	v_perm_b32 v152, v152, v147, s36
	v_perm_b32 v156, v153, v149, s35
	v_perm_b32 v160, v153, v149, s36
	s_waitcnt lgkmcnt(0)
	v_perm_b32 v147, v151, v150, s33
	v_perm_b32 v158, v151, v150, s34
	v_perm_b32 v153, v155, v154, s33
	v_perm_b32 v159, v155, v154, s34
	ds_read2_b32 v[150:151], v137 offset0:72 offset1:81
	ds_read2_b32 v[154:155], v137 offset0:90 offset1:99
	v_perm_b32 v149, v153, v147, s35
	v_perm_b32 v153, v153, v147, s36
	v_perm_b32 v157, v159, v158, s35
	v_perm_b32 v161, v159, v158, s36
	s_waitcnt lgkmcnt(1)
	v_perm_b32 v147, v151, v150, s33
	s_waitcnt lgkmcnt(0)
	v_perm_b32 v158, v155, v154, s33
	v_perm_b32 v151, v151, v150, s34
	v_perm_b32 v155, v155, v154, s34
	v_perm_b32 v150, v158, v147, s35
	v_perm_b32 v154, v158, v147, s36
	v_perm_b32 v147, v165, v164, s33
	v_perm_b32 v163, v165, v164, s34
	v_perm_b32 v164, v167, v166, s34
	v_perm_b32 v159, v164, v163, s35
	v_perm_b32 v163, v164, v163, s36
	v_or_b32_e32 v164, s1, v135
	s_addc_u32 s1, s12, 0
	v_perm_b32 v158, v155, v151, s35
	v_perm_b32 v162, v155, v151, s36
	v_perm_b32 v155, v167, v166, s33
	v_lshl_add_u64 v[166:167], s[0:1], 0, v[132:133]
	v_mov_b32_e32 v165, v131
	v_perm_b32 v151, v155, v147, s35
	v_lshl_add_u64 v[164:165], v[166:167], 0, v[164:165]
	v_perm_b32 v155, v155, v147, s36
	global_store_dwordx4 v[164:165], v[148:151], off nt
	global_store_dwordx4 v[164:165], v[152:155], off offset:2048 nt
	s_nop 0
	v_add_co_u32_e32 v148, vcc, 0x1000, v164
	s_nop 1
	v_addc_co_u32_e32 v149, vcc, 0, v165, vcc
	global_store_dwordx4 v[148:149], v[156:159], off nt
	global_store_dwordx4 v[148:149], v[160:163], off offset:2048 nt
	s_waitcnt lgkmcnt(0)
	s_cbranch_execz .LBB0_910

.LBB0_910:
	s_cmp_gt_i32 s42, 0x17fff
	s_cbranch_scc1 .Lcvw_a2_drain
	s_waitcnt vmcnt(16)
	s_branch .Lcvw_a2_go

.Lcvw_a2_go:
	v_pk_mul_f32 v[148:149], v[6:7], s[10:11] op_sel_hi:[1,0]
	v_mov_b32_e32 v147, v131
	v_cvt_pk_fp8_f32 v147, v148, v149
	v_pk_mul_f32 v[148:149], v[2:3], s[10:11] op_sel_hi:[1,0]
	v_mov_b32_e32 v150, v131
	v_cvt_pk_fp8_f32 v150, v148, v149
	v_pk_mul_f32 v[148:149], v[8:9], s[10:11] op_sel_hi:[1,0]
	v_mov_b32_e32 v151, v131
	v_cvt_pk_fp8_f32 v147, v148, v149 op_sel:[0,0,1]
	v_pk_mul_f32 v[148:149], v[4:5], s[10:11] op_sel_hi:[1,0]
	v_mov_b32_e32 v152, v131
	v_cvt_pk_fp8_f32 v150, v148, v149 op_sel:[0,0,1]
	v_pk_mul_f32 v[148:149], v[10:11], s[10:11] op_sel_hi:[1,0]
	v_mov_b32_e32 v153, v131
	v_cvt_pk_fp8_f32 v151, v148, v149
	v_pk_mul_f32 v[148:149], v[14:15], s[10:11] op_sel_hi:[1,0]
	v_mov_b32_e32 v154, v131
	v_cvt_pk_fp8_f32 v152, v148, v149
	v_pk_mul_f32 v[148:149], v[12:13], s[10:11] op_sel_hi:[1,0]
	v_mov_b32_e32 v155, v131
	v_cvt_pk_fp8_f32 v151, v148, v149 op_sel:[0,0,1]
	v_pk_mul_f32 v[148:149], v[16:17], s[10:11] op_sel_hi:[1,0]
	v_mov_b32_e32 v156, v131
	v_cvt_pk_fp8_f32 v152, v148, v149 op_sel:[0,0,1]
	v_pk_mul_f32 v[148:149], v[18:19], s[10:11] op_sel_hi:[1,0]
	s_ashr_i32 s0, s22, 31
	v_cvt_pk_fp8_f32 v153, v148, v149
	v_pk_mul_f32 v[148:149], v[22:23], s[10:11] op_sel_hi:[1,0]
	s_lshr_b32 s0, s0, 21
	v_cvt_pk_fp8_f32 v154, v148, v149
	v_pk_mul_f32 v[148:149], v[20:21], s[10:11] op_sel_hi:[1,0]
	s_add_i32 s1, s22, s0
	v_cvt_pk_fp8_f32 v153, v148, v149 op_sel:[0,0,1]
	v_pk_mul_f32 v[148:149], v[24:25], s[10:11] op_sel_hi:[1,0]
	s_ashr_i32 s0, s1, 11
	v_cvt_pk_fp8_f32 v154, v148, v149 op_sel:[0,0,1]
	v_pk_mul_f32 v[148:149], v[26:27], s[10:11] op_sel_hi:[1,0]
	s_and_b32 s1, s1, 0xf800
	v_cvt_pk_fp8_f32 v155, v148, v149
	v_pk_mul_f32 v[148:149], v[30:31], s[10:11] op_sel_hi:[1,0]
	s_sub_i32 s1, s22, s1
	v_cvt_pk_fp8_f32 v156, v148, v149
	v_pk_mul_f32 v[148:149], v[28:29], s[10:11] op_sel_hi:[1,0]
	s_sext_i32_i16 s8, s1
	v_cvt_pk_fp8_f32 v155, v148, v149 op_sel:[0,0,1]
	v_pk_mul_f32 v[148:149], v[32:33], s[10:11] op_sel_hi:[1,0]
	s_bfe_u32 s8, s8, 0x70018
	v_cvt_pk_fp8_f32 v156, v148, v149 op_sel:[0,0,1]
	ds_write2_b32 v136, v147, v150 offset1:72
	ds_write2_b32 v136, v151, v152 offset0:144 offset1:216
	ds_write2_b32 v146, v153, v154 offset0:32 offset1:104
	ds_write2_b32 v146, v155, v156 offset0:176 offset1:248
	v_pk_mul_f32 v[148:149], v[34:35], s[10:11] op_sel_hi:[1,0]
	v_mov_b32_e32 v147, v131
	v_cvt_pk_fp8_f32 v147, v148, v149
	v_pk_mul_f32 v[148:149], v[38:39], s[10:11] op_sel_hi:[1,0]
	v_mov_b32_e32 v150, v131
	v_cvt_pk_fp8_f32 v150, v148, v149
	v_pk_mul_f32 v[148:149], v[36:37], s[10:11] op_sel_hi:[1,0]
	v_mov_b32_e32 v151, v131
	v_cvt_pk_fp8_f32 v147, v148, v149 op_sel:[0,0,1]
	v_pk_mul_f32 v[148:149], v[40:41], s[10:11] op_sel_hi:[1,0]
	v_mov_b32_e32 v152, v131
	v_cvt_pk_fp8_f32 v150, v148, v149 op_sel:[0,0,1]
	v_pk_mul_f32 v[148:149], v[50:51], s[10:11] op_sel_hi:[1,0]
	v_mov_b32_e32 v153, v131
	v_cvt_pk_fp8_f32 v151, v148, v149
	v_pk_mul_f32 v[148:149], v[54:55], s[10:11] op_sel_hi:[1,0]
	v_mov_b32_e32 v154, v131
	v_cvt_pk_fp8_f32 v152, v148, v149
	v_pk_mul_f32 v[148:149], v[52:53], s[10:11] op_sel_hi:[1,0]
	v_mov_b32_e32 v155, v131
	v_cvt_pk_fp8_f32 v151, v148, v149 op_sel:[0,0,1]
	v_pk_mul_f32 v[148:149], v[56:57], s[10:11] op_sel_hi:[1,0]
	v_mov_b32_e32 v156, v131
	v_cvt_pk_fp8_f32 v152, v148, v149 op_sel:[0,0,1]
	v_pk_mul_f32 v[148:149], v[66:67], s[10:11] op_sel_hi:[1,0]
	s_add_i32 s12, s1, s8
	v_cvt_pk_fp8_f32 v153, v148, v149
	v_pk_mul_f32 v[148:149], v[74:75], s[10:11] op_sel_hi:[1,0]
	s_sext_i32_i16 s8, s12
	v_cvt_pk_fp8_f32 v154, v148, v149
	v_pk_mul_f32 v[148:149], v[68:69], s[10:11] op_sel_hi:[1,0]
	s_and_b32 s12, s12, 0xff80
	v_cvt_pk_fp8_f32 v153, v148, v149 op_sel:[0,0,1]
	v_pk_mul_f32 v[148:149], v[76:77], s[10:11] op_sel_hi:[1,0]
	s_sub_i32 s1, s1, s12
	v_cvt_pk_fp8_f32 v154, v148, v149 op_sel:[0,0,1]
	v_pk_mul_f32 v[148:149], v[86:87], s[10:11] op_sel_hi:[1,0]
	s_sext_i32_i16 s12, s1
	v_cvt_pk_fp8_f32 v155, v148, v149
	v_pk_mul_f32 v[148:149], v[94:95], s[10:11] op_sel_hi:[1,0]
	s_ashr_i32 s1, s0, 31
	v_cvt_pk_fp8_f32 v156, v148, v149
	v_pk_mul_f32 v[148:149], v[88:89], s[10:11] op_sel_hi:[1,0]
	s_and_b32 s8, s8, 0xffffff80
	v_cvt_pk_fp8_f32 v155, v148, v149 op_sel:[0,0,1]
	v_pk_mul_f32 v[148:149], v[96:97], s[10:11] op_sel_hi:[1,0]
	s_lshl_b64 s[0:1], s[0:1], 23
	v_cvt_pk_fp8_f32 v156, v148, v149 op_sel:[0,0,1]
	ds_write2_b32 v142, v147, v150 offset0:64 offset1:136
	ds_write2_b32 v143, v151, v152 offset0:80 offset1:152
	ds_write2_b32 v144, v153, v154 offset0:96 offset1:168
	ds_write2_b32 v145, v155, v156 offset0:112 offset1:184
	s_waitcnt lgkmcnt(0)
	ds_read2_b32 v[150:151], v137 offset0:18 offset1:27
	ds_read2_b32 v[148:149], v137 offset1:9
	ds_read2_b32 v[154:155], v137 offset0:54 offset1:63
	ds_read2_b32 v[164:165], v137 offset0:108 offset1:117
	ds_read2_b32 v[166:167], v137 offset0:126 offset1:135
	s_waitcnt lgkmcnt(4)
	v_perm_b32 v152, v151, v150, s33
	v_perm_b32 v153, v151, v150, s34
	ds_read2_b32 v[150:151], v137 offset0:36 offset1:45
	s_waitcnt lgkmcnt(4)
	v_perm_b32 v147, v149, v148, s33
	v_perm_b32 v149, v149, v148, s34
	v_perm_b32 v148, v152, v147, s35
	v_perm_b32 v152, v152, v147, s36
	v_perm_b32 v156, v153, v149, s35
	v_perm_b32 v160, v153, v149, s36
	s_waitcnt lgkmcnt(0)
	v_perm_b32 v147, v151, v150, s33
	v_perm_b32 v158, v151, v150, s34
	v_perm_b32 v153, v155, v154, s33
	v_perm_b32 v159, v155, v154, s34
	ds_read2_b32 v[150:151], v137 offset0:72 offset1:81
	ds_read2_b32 v[154:155], v137 offset0:90 offset1:99
	v_perm_b32 v149, v153, v147, s35
	v_perm_b32 v153, v153, v147, s36
	v_perm_b32 v157, v159, v158, s35
	v_perm_b32 v161, v159, v158, s36
	s_waitcnt lgkmcnt(1)
	v_perm_b32 v147, v151, v150, s33
	v_perm_b32 v151, v151, v150, s34
	s_waitcnt lgkmcnt(0)
	v_perm_b32 v158, v155, v154, s33
	v_perm_b32 v155, v155, v154, s34
	v_perm_b32 v150, v158, v147, s35
	v_perm_b32 v154, v158, v147, s36
	v_perm_b32 v158, v155, v151, s35
	v_perm_b32 v162, v155, v151, s36
	v_perm_b32 v147, v165, v164, s33
	v_perm_b32 v155, v167, v166, s33
	v_perm_b32 v151, v155, v147, s35
	v_perm_b32 v155, v155, v147, s36
	v_lshl_or_b32 v147, s12, 5, v134
	v_perm_b32 v163, v165, v164, s34
	v_perm_b32 v164, v167, v166, s34
	v_add_u32_e32 v166, 0xfffff800, v147
	v_cmp_lt_i32_e32 vcc, s37, v147
	s_add_u32 s0, s16, s0
	s_addc_u32 s1, s17, s1
	v_cndmask_b32_e32 v166, v147, v166, vcc
	v_lshlrev_b32_e32 v167, 1, v166
	s_ashr_i32 s12, s8, 31
	v_and_b32_e32 v167, 0xffffff00, v167
	v_cndmask_b32_e32 v168, 0, v138, vcc
	v_and_b32_e32 v166, 0x7c, v166
	s_add_u32 s0, s0, s8
	v_or3_b32 v166, v166, v168, v167
	s_addc_u32 s1, s1, s12
	v_ashrrev_i32_e32 v167, 31, v166
	v_perm_b32 v159, v164, v163, s35
	v_perm_b32 v163, v164, v163, s36
	v_lshl_add_u64 v[164:165], s[0:1], 0, v[132:133]
	v_lshlrev_b64 v[166:167], 11, v[166:167]
	v_lshl_add_u64 v[166:167], v[164:165], 0, v[166:167]
	v_cmp_lt_i32_e32 vcc, s38, v147
	global_store_dwordx4 v[166:167], v[148:151], off nt
	s_nop 1
	v_cndmask_b32_e32 v148, 1, v139, vcc
	v_add_u32_e32 v148, v148, v147
	v_lshlrev_b32_e32 v149, 1, v148
	v_and_b32_e32 v149, 0xffffff00, v149
	v_cndmask_b32_e32 v150, 0, v138, vcc
	v_and_b32_e32 v148, 0x7d, v148
	v_or3_b32 v148, v148, v150, v149
	v_ashrrev_i32_e32 v149, 31, v148
	v_lshlrev_b64 v[148:149], 11, v[148:149]
	v_lshl_add_u64 v[148:149], v[164:165], 0, v[148:149]
	v_cmp_lt_i32_e32 vcc, s39, v147
	global_store_dwordx4 v[148:149], v[152:155], off nt
	s_nop 0
	v_cndmask_b32_e32 v148, 2, v140, vcc
	v_add_u32_e32 v148, v148, v147
	v_lshlrev_b32_e32 v149, 1, v148
	v_and_b32_e32 v149, 0xffffff00, v149
	v_cndmask_b32_e32 v150, 0, v138, vcc
	v_and_b32_e32 v148, 0x7e, v148
	v_or3_b32 v148, v148, v150, v149
	v_ashrrev_i32_e32 v149, 31, v148
	v_lshlrev_b64 v[148:149], 11, v[148:149]
	v_lshl_add_u64 v[148:149], v[164:165], 0, v[148:149]
	v_cmp_lt_i32_e32 vcc, s40, v147
	global_store_dwordx4 v[148:149], v[156:159], off nt
	s_nop 0
	v_cndmask_b32_e32 v148, 3, v141, vcc
	v_add_u32_e32 v147, v148, v147
	v_lshlrev_b32_e32 v148, 1, v147
	v_and_b32_e32 v148, 0xffffff00, v148
	v_cndmask_b32_e32 v149, 0, v138, vcc
	v_and_b32_e32 v147, 0x7f, v147
	v_or3_b32 v148, v147, v149, v148
	v_ashrrev_i32_e32 v149, 31, v148
	v_lshlrev_b64 v[148:149], 11, v[148:149]
	v_lshl_add_u64 v[148:149], v[164:165], 0, v[148:149]
	global_store_dwordx4 v[148:149], v[160:163], off nt
	s_waitcnt lgkmcnt(0)
	s_cmp_gt_i32 s42, 0x17fff
	s_mov_b64 s[12:13], -1
	s_cbranch_scc1 .LBB0_896

.LBB0_915:
	s_or_b64 exec, exec, s[0:1]
	v_mov_b32_e32 v147, s41
	s_waitcnt lgkmcnt(0)
	s_barrier
	ds_read_b32 v147, v147
	s_waitcnt lgkmcnt(0)
	v_readfirstlane_b32 s0, v147
	s_add_i32 s22, s0, s2
	s_cmp_gt_i32 s22, 0x17fff
	s_cselect_b64 s[12:13], -1, 0
	s_and_b64 vcc, exec, s[12:13]
	s_cbranch_vccnz .LBB0_920
	s_cmp_gt_i32 s22, 0xffff
	s_mov_b64 s[0:1], -1
	s_cbranch_scc0 .LBB0_918
	s_load_dwordx2 s[0:1], s[46:47], 0xe0
	s_add_i32 s8, s22, 0xffff0000
	s_lshr_b32 s8, s8, 10
	s_lshl_b64 s[14:15], s[8:9], 24
	v_mov_b32_e32 v5, v131
	s_waitcnt lgkmcnt(0)
	s_add_u32 s0, s0, s14
	s_addc_u32 s1, s1, s15
	s_lshl_b32 s8, s22, 1
	s_and_b32 s8, s8, 0x780
	v_or_b32_e32 v4, s8, v1
	s_lshl_b32 s8, s22, 7
	s_and_b32 s8, s8, 0x1f80
	s_add_u32 s0, s0, s8
	s_addc_u32 s1, s1, 0
	v_lshl_add_u64 v[2:3], s[0:1], 0, v[130:131]
	v_lshlrev_b32_e32 v4, 13, v4
	v_lshl_add_u64 v[86:87], v[2:3], 0, v[4:5]
	v_add_co_u32_e32 v2, vcc, s19, v86
	s_mov_b64 s[0:1], 0
	s_nop 0
	v_addc_co_u32_e32 v3, vcc, 0, v87, vcc
	v_add_co_u32_e32 v10, vcc, s20, v86
	global_load_dwordx4 v[6:9], v[86:87], off nt
	s_nop 0
	global_load_dwordx4 v[2:5], v[2:3], off nt
	v_addc_co_u32_e32 v11, vcc, 0, v87, vcc
	v_add_co_u32_e32 v14, vcc, s21, v86
	s_nop 1
	v_addc_co_u32_e32 v15, vcc, 0, v87, vcc
	v_add_co_u32_e32 v18, vcc, s23, v86
	global_load_dwordx4 v[10:13], v[10:11], off nt
	s_nop 0
	global_load_dwordx4 v[14:17], v[14:15], off nt
	v_addc_co_u32_e32 v19, vcc, 0, v87, vcc
	v_add_co_u32_e32 v22, vcc, s24, v86
	s_nop 1
	v_addc_co_u32_e32 v23, vcc, 0, v87, vcc
	v_add_co_u32_e32 v26, vcc, s25, v86
	global_load_dwordx4 v[18:21], v[18:19], off nt
	s_nop 0
	global_load_dwordx4 v[22:25], v[22:23], off nt
	v_addc_co_u32_e32 v27, vcc, 0, v87, vcc
	v_add_co_u32_e32 v30, vcc, s26, v86
	s_nop 1
	v_addc_co_u32_e32 v31, vcc, 0, v87, vcc
	v_add_co_u32_e32 v34, vcc, s27, v86
	global_load_dwordx4 v[26:29], v[26:27], off nt
	s_nop 0
	global_load_dwordx4 v[30:33], v[30:31], off nt
	v_addc_co_u32_e32 v35, vcc, 0, v87, vcc
	v_add_co_u32_e32 v38, vcc, s28, v86
	s_nop 1
	v_addc_co_u32_e32 v39, vcc, 0, v87, vcc
	v_add_co_u32_e32 v50, vcc, s29, v86
	global_load_dwordx4 v[34:37], v[34:35], off nt
	s_nop 0
	global_load_dwordx4 v[38:41], v[38:39], off nt
	v_addc_co_u32_e32 v51, vcc, 0, v87, vcc
	v_add_co_u32_e32 v54, vcc, s30, v86
	s_nop 1
	v_addc_co_u32_e32 v55, vcc, 0, v87, vcc
	v_add_co_u32_e32 v66, vcc, s31, v86
	global_load_dwordx4 v[50:53], v[50:51], off nt
	s_nop 0
	global_load_dwordx4 v[54:57], v[54:55], off nt
	v_addc_co_u32_e32 v67, vcc, 0, v87, vcc
	v_add_co_u32_e32 v74, vcc, 0xd0000, v86
	s_nop 1
	v_addc_co_u32_e32 v75, vcc, 0, v87, vcc
	v_add_co_u32_e32 v88, vcc, 0xe0000, v86
	global_load_dwordx4 v[66:69], v[66:67], off nt
	s_nop 0
	global_load_dwordx4 v[74:77], v[74:75], off nt
	v_addc_co_u32_e32 v89, vcc, 0, v87, vcc
	v_add_co_u32_e32 v94, vcc, 0xf0000, v86
	s_nop 1
	v_addc_co_u32_e32 v95, vcc, 0, v87, vcc
	global_load_dwordx4 v[86:89], v[88:89], off nt
	s_nop 0
	global_load_dwordx4 v[94:97], v[94:95], off nt
.LBB0_918:
	s_andn2_b64 vcc, exec, s[0:1]
	s_cbranch_vccnz .LBB0_920
	s_ashr_i32 s0, s22, 31
	s_lshr_b32 s0, s0, 21
	s_load_dwordx2 s[14:15], s[46:47], 0xd0
	s_add_i32 s1, s22, s0
	s_ashr_i32 s0, s1, 11
	s_and_b32 s1, s1, 0xf800
	s_sub_i32 s8, s22, s1
	s_ashr_i32 s1, s0, 31
	s_lshl_b64 s[0:1], s[0:1], 25
	s_waitcnt lgkmcnt(0)
	s_add_u32 s14, s14, s0
	s_sext_i32_i16 s0, s8
	s_addc_u32 s15, s15, s1
	s_bfe_u32 s0, s0, 0x70018
	s_add_i32 s0, s8, s0
	s_sext_i32_i16 s1, s0
	s_and_b32 s0, s0, 0xff80
	s_sub_i32 s0, s8, s0
	s_sext_i32_i16 s0, s0
	s_and_b32 s1, s1, 0xffffff80
	s_lshl_b32 s0, s0, 5
	v_or_b32_e32 v86, s1, v1
	s_ashr_i32 s1, s0, 31
	s_lshl_b64 s[0:1], s[0:1], 2
	v_ashrrev_i32_e32 v87, 31, v86
	s_add_u32 s0, s14, s0
	v_lshlrev_b64 v[2:3], 14, v[86:87]
	v_or_b32_e32 v4, 8, v86
	v_or_b32_e32 v10, 16, v86
	v_or_b32_e32 v12, 24, v86
	v_or_b32_e32 v18, 32, v86
	v_or_b32_e32 v20, 40, v86
	v_or_b32_e32 v26, 48, v86
	v_or_b32_e32 v28, 56, v86
	v_or_b32_e32 v34, 64, v86
	v_or_b32_e32 v36, 0x48, v86
	v_or_b32_e32 v50, 0x50, v86
	v_or_b32_e32 v52, 0x58, v86
	v_or_b32_e32 v66, 0x60, v86
	v_or_b32_e32 v68, 0x68, v86
	v_or_b32_e32 v94, 0x70, v86
	v_or_b32_e32 v86, 0x78, v86
	s_addc_u32 s1, s15, s1
	v_ashrrev_i32_e32 v5, 31, v4
	v_ashrrev_i32_e32 v11, 31, v10
	v_ashrrev_i32_e32 v13, 31, v12
	v_ashrrev_i32_e32 v19, 31, v18
	v_ashrrev_i32_e32 v21, 31, v20
	v_ashrrev_i32_e32 v27, 31, v26
	v_ashrrev_i32_e32 v29, 31, v28
	v_ashrrev_i32_e32 v35, 31, v34
	v_ashrrev_i32_e32 v37, 31, v36
	v_ashrrev_i32_e32 v51, 31, v50
	v_ashrrev_i32_e32 v53, 31, v52
	v_ashrrev_i32_e32 v67, 31, v66
	v_ashrrev_i32_e32 v69, 31, v68
	v_ashrrev_i32_e32 v95, 31, v94
	v_ashrrev_i32_e32 v87, 31, v86
	v_lshl_add_u64 v[88:89], s[0:1], 0, v[130:131]
	v_lshlrev_b64 v[4:5], 14, v[4:5]
	v_lshlrev_b64 v[10:11], 14, v[10:11]
	v_lshlrev_b64 v[12:13], 14, v[12:13]
	v_lshlrev_b64 v[18:19], 14, v[18:19]
	v_lshlrev_b64 v[20:21], 14, v[20:21]
	v_lshlrev_b64 v[26:27], 14, v[26:27]
	v_lshlrev_b64 v[28:29], 14, v[28:29]
	v_lshlrev_b64 v[34:35], 14, v[34:35]
	v_lshlrev_b64 v[36:37], 14, v[36:37]
	v_lshlrev_b64 v[50:51], 14, v[50:51]
	v_lshlrev_b64 v[52:53], 14, v[52:53]
	v_lshlrev_b64 v[66:67], 14, v[66:67]
	v_lshlrev_b64 v[68:69], 14, v[68:69]
	v_lshlrev_b64 v[94:95], 14, v[94:95]
	v_lshlrev_b64 v[86:87], 14, v[86:87]
	v_lshl_add_u64 v[2:3], v[88:89], 0, v[2:3]
	v_lshl_add_u64 v[4:5], v[88:89], 0, v[4:5]
	v_lshl_add_u64 v[10:11], v[88:89], 0, v[10:11]
	v_lshl_add_u64 v[14:15], v[88:89], 0, v[12:13]
	v_lshl_add_u64 v[18:19], v[88:89], 0, v[18:19]
	v_lshl_add_u64 v[22:23], v[88:89], 0, v[20:21]
	v_lshl_add_u64 v[26:27], v[88:89], 0, v[26:27]
	v_lshl_add_u64 v[30:31], v[88:89], 0, v[28:29]
	v_lshl_add_u64 v[34:35], v[88:89], 0, v[34:35]
	v_lshl_add_u64 v[38:39], v[88:89], 0, v[36:37]
	v_lshl_add_u64 v[50:51], v[88:89], 0, v[50:51]
	v_lshl_add_u64 v[54:55], v[88:89], 0, v[52:53]
	v_lshl_add_u64 v[66:67], v[88:89], 0, v[66:67]
	v_lshl_add_u64 v[74:75], v[88:89], 0, v[68:69]
	v_lshl_add_u64 v[94:95], v[88:89], 0, v[94:95]
	v_lshl_add_u64 v[96:97], v[88:89], 0, v[86:87]
	global_load_dwordx4 v[6:9], v[2:3], off nt
	s_nop 0
	global_load_dwordx4 v[2:5], v[4:5], off nt
	s_nop 0
	global_load_dwordx4 v[10:13], v[10:11], off nt
	s_nop 0
	global_load_dwordx4 v[14:17], v[14:15], off nt
	s_nop 0
	global_load_dwordx4 v[18:21], v[18:19], off nt
	s_nop 0
	global_load_dwordx4 v[22:25], v[22:23], off nt
	s_nop 0
	global_load_dwordx4 v[26:29], v[26:27], off nt
	s_nop 0
	global_load_dwordx4 v[30:33], v[30:31], off nt
	s_nop 0
	global_load_dwordx4 v[34:37], v[34:35], off nt
	s_nop 0
	global_load_dwordx4 v[38:41], v[38:39], off nt
	s_nop 0
	global_load_dwordx4 v[50:53], v[50:51], off nt
	s_nop 0
	global_load_dwordx4 v[54:57], v[54:55], off nt
	s_nop 0
	global_load_dwordx4 v[66:69], v[66:67], off nt
	s_nop 0
	global_load_dwordx4 v[74:77], v[74:75], off nt
	s_nop 0
	global_load_dwordx4 v[86:89], v[94:95], off nt
	s_nop 0
	global_load_dwordx4 v[94:97], v[96:97], off nt
.LBB0_920:
	s_cmp_gt_i32 s42, 0xffff
	s_mov_b64 s[0:1], -1
	s_cbranch_scc0 .LBB0_922
	s_cmp_gt_i32 s22, 0x17fff
	s_cbranch_scc1 .Lcvw_b1_drain
	s_waitcnt vmcnt(20)
	s_branch .Lcvw_b1_go

.Lcvw_b1_go:
	v_pk_mul_f32 v[148:149], v[42:43], s[10:11] op_sel_hi:[1,0]
	v_mov_b32_e32 v147, v131
	v_cvt_pk_fp8_f32 v147, v148, v149
	v_pk_mul_f32 v[148:149], v[46:47], s[10:11] op_sel_hi:[1,0]
	v_mov_b32_e32 v150, v131
	v_cvt_pk_fp8_f32 v150, v148, v149
	v_pk_mul_f32 v[148:149], v[44:45], s[10:11] op_sel_hi:[1,0]
	v_mov_b32_e32 v151, v131
	v_cvt_pk_fp8_f32 v147, v148, v149 op_sel:[0,0,1]
	v_pk_mul_f32 v[148:149], v[48:49], s[10:11] op_sel_hi:[1,0]
	v_mov_b32_e32 v152, v131
	v_cvt_pk_fp8_f32 v150, v148, v149 op_sel:[0,0,1]
	v_pk_mul_f32 v[148:149], v[58:59], s[10:11] op_sel_hi:[1,0]
	v_mov_b32_e32 v153, v131
	v_cvt_pk_fp8_f32 v151, v148, v149
	v_pk_mul_f32 v[148:149], v[62:63], s[10:11] op_sel_hi:[1,0]
	v_mov_b32_e32 v154, v131
	v_cvt_pk_fp8_f32 v152, v148, v149
	v_pk_mul_f32 v[148:149], v[60:61], s[10:11] op_sel_hi:[1,0]
	v_mov_b32_e32 v155, v131
	v_cvt_pk_fp8_f32 v151, v148, v149 op_sel:[0,0,1]
	v_pk_mul_f32 v[148:149], v[64:65], s[10:11] op_sel_hi:[1,0]
	v_mov_b32_e32 v156, v131
	v_cvt_pk_fp8_f32 v152, v148, v149 op_sel:[0,0,1]
	v_pk_mul_f32 v[148:149], v[70:71], s[10:11] op_sel_hi:[1,0]
	s_add_i32 s0, s42, 0xffff0000
	v_cvt_pk_fp8_f32 v153, v148, v149
	v_pk_mul_f32 v[148:149], v[78:79], s[10:11] op_sel_hi:[1,0]
	s_lshr_b32 s8, s0, 10
	v_cvt_pk_fp8_f32 v154, v148, v149
	v_pk_mul_f32 v[148:149], v[72:73], s[10:11] op_sel_hi:[1,0]
	s_lshl_b32 s0, s42, 1
	v_cvt_pk_fp8_f32 v153, v148, v149 op_sel:[0,0,1]
	v_pk_mul_f32 v[148:149], v[80:81], s[10:11] op_sel_hi:[1,0]
	s_lshl_b32 s1, s42, 16
	v_cvt_pk_fp8_f32 v154, v148, v149 op_sel:[0,0,1]
	v_pk_mul_f32 v[148:149], v[82:83], s[10:11] op_sel_hi:[1,0]
	s_and_b32 s0, s0, 0x780
	v_cvt_pk_fp8_f32 v155, v148, v149
	v_pk_mul_f32 v[148:149], v[90:91], s[10:11] op_sel_hi:[1,0]
	s_and_b32 s1, s1, 0x3f0000
	v_cvt_pk_fp8_f32 v156, v148, v149
	v_pk_mul_f32 v[148:149], v[84:85], s[10:11] op_sel_hi:[1,0]
	s_lshl_b64 s[14:15], s[8:9], 22
	v_cvt_pk_fp8_f32 v155, v148, v149 op_sel:[0,0,1]
	v_pk_mul_f32 v[148:149], v[92:93], s[10:11] op_sel_hi:[1,0]
	s_add_u32 s8, s3, s14
	v_cvt_pk_fp8_f32 v156, v148, v149 op_sel:[0,0,1]
	ds_write2_b32 v136, v147, v150 offset1:72
	ds_write2_b32 v136, v151, v152 offset0:144 offset1:216
	ds_write2_b32 v146, v153, v154 offset0:32 offset1:104
	ds_write2_b32 v146, v155, v156 offset0:176 offset1:248
	v_pk_mul_f32 v[148:149], v[98:99], s[10:11] op_sel_hi:[1,0]
	v_mov_b32_e32 v147, v131
	v_cvt_pk_fp8_f32 v147, v148, v149
	v_pk_mul_f32 v[148:149], v[102:103], s[10:11] op_sel_hi:[1,0]
	v_mov_b32_e32 v150, v131
	v_cvt_pk_fp8_f32 v150, v148, v149
	v_pk_mul_f32 v[148:149], v[100:101], s[10:11] op_sel_hi:[1,0]
	v_mov_b32_e32 v151, v131
	v_cvt_pk_fp8_f32 v147, v148, v149 op_sel:[0,0,1]
	v_pk_mul_f32 v[148:149], v[104:105], s[10:11] op_sel_hi:[1,0]
	v_mov_b32_e32 v152, v131
	v_cvt_pk_fp8_f32 v150, v148, v149 op_sel:[0,0,1]
	v_pk_mul_f32 v[148:149], v[106:107], s[10:11] op_sel_hi:[1,0]
	v_mov_b32_e32 v153, v131
	v_cvt_pk_fp8_f32 v151, v148, v149
	v_pk_mul_f32 v[148:149], v[110:111], s[10:11] op_sel_hi:[1,0]
	v_mov_b32_e32 v154, v131
	v_cvt_pk_fp8_f32 v152, v148, v149
	v_pk_mul_f32 v[148:149], v[108:109], s[10:11] op_sel_hi:[1,0]
	v_mov_b32_e32 v155, v131
	v_cvt_pk_fp8_f32 v151, v148, v149 op_sel:[0,0,1]
	v_pk_mul_f32 v[148:149], v[112:113], s[10:11] op_sel_hi:[1,0]
	v_mov_b32_e32 v156, v131
	v_cvt_pk_fp8_f32 v152, v148, v149 op_sel:[0,0,1]
	v_pk_mul_f32 v[148:149], v[114:115], s[10:11] op_sel_hi:[1,0]
	s_addc_u32 s14, s11, s15
	v_cvt_pk_fp8_f32 v153, v148, v149
	v_pk_mul_f32 v[148:149], v[118:119], s[10:11] op_sel_hi:[1,0]
	s_add_u32 s0, s8, s0
	v_cvt_pk_fp8_f32 v154, v148, v149
	v_pk_mul_f32 v[148:149], v[116:117], s[10:11] op_sel_hi:[1,0]
	s_nop 0
	v_cvt_pk_fp8_f32 v153, v148, v149 op_sel:[0,0,1]
	v_pk_mul_f32 v[148:149], v[120:121], s[10:11] op_sel_hi:[1,0]
	s_nop 0
	v_cvt_pk_fp8_f32 v154, v148, v149 op_sel:[0,0,1]
	v_pk_mul_f32 v[148:149], v[122:123], s[10:11] op_sel_hi:[1,0]
	s_nop 0
	v_cvt_pk_fp8_f32 v155, v148, v149
	v_pk_mul_f32 v[148:149], v[126:127], s[10:11] op_sel_hi:[1,0]
	s_nop 0
	v_cvt_pk_fp8_f32 v156, v148, v149
	v_pk_mul_f32 v[148:149], v[124:125], s[10:11] op_sel_hi:[1,0]
	s_nop 0
	v_cvt_pk_fp8_f32 v155, v148, v149 op_sel:[0,0,1]
	v_pk_mul_f32 v[148:149], v[128:129], s[10:11] op_sel_hi:[1,0]
	s_nop 0
	v_cvt_pk_fp8_f32 v156, v148, v149 op_sel:[0,0,1]
	ds_write2_b32 v142, v147, v150 offset0:64 offset1:136
	ds_write2_b32 v143, v151, v152 offset0:80 offset1:152
	ds_write2_b32 v144, v153, v154 offset0:96 offset1:168
	ds_write2_b32 v145, v155, v156 offset0:112 offset1:184
	s_waitcnt lgkmcnt(0)
	ds_read2_b32 v[150:151], v137 offset0:18 offset1:27
	ds_read2_b32 v[148:149], v137 offset1:9
	ds_read2_b32 v[154:155], v137 offset0:54 offset1:63
	ds_read2_b32 v[164:165], v137 offset0:108 offset1:117
	ds_read2_b32 v[166:167], v137 offset0:126 offset1:135
	s_waitcnt lgkmcnt(4)
	v_perm_b32 v152, v151, v150, s33
	v_perm_b32 v153, v151, v150, s34
	ds_read2_b32 v[150:151], v137 offset0:36 offset1:45
	s_waitcnt lgkmcnt(4)
	v_perm_b32 v147, v149, v148, s33
	v_perm_b32 v149, v149, v148, s34
	v_perm_b32 v148, v152, v147, s35
	v_perm_b32 v152, v152, v147, s36
	v_perm_b32 v156, v153, v149, s35
	v_perm_b32 v160, v153, v149, s36
	s_waitcnt lgkmcnt(0)
	v_perm_b32 v147, v151, v150, s33
	v_perm_b32 v158, v151, v150, s34
	v_perm_b32 v153, v155, v154, s33
	v_perm_b32 v159, v155, v154, s34
	ds_read2_b32 v[150:151], v137 offset0:72 offset1:81
	ds_read2_b32 v[154:155], v137 offset0:90 offset1:99
	v_perm_b32 v149, v153, v147, s35
	v_perm_b32 v153, v153, v147, s36
	v_perm_b32 v157, v159, v158, s35
	v_perm_b32 v161, v159, v158, s36
	s_waitcnt lgkmcnt(1)
	v_perm_b32 v147, v151, v150, s33
	s_waitcnt lgkmcnt(0)
	v_perm_b32 v158, v155, v154, s33
	v_perm_b32 v151, v151, v150, s34
	v_perm_b32 v155, v155, v154, s34
	v_perm_b32 v150, v158, v147, s35
	v_perm_b32 v154, v158, v147, s36
	v_perm_b32 v147, v165, v164, s33
	v_perm_b32 v163, v165, v164, s34
	v_perm_b32 v164, v167, v166, s34
	v_perm_b32 v159, v164, v163, s35
	v_perm_b32 v163, v164, v163, s36
	v_or_b32_e32 v164, s1, v135
	s_addc_u32 s1, s14, 0
	v_perm_b32 v158, v155, v151, s35
	v_perm_b32 v162, v155, v151, s36
	v_perm_b32 v155, v167, v166, s33
	v_lshl_add_u64 v[166:167], s[0:1], 0, v[132:133]
	v_mov_b32_e32 v165, v131
	v_perm_b32 v151, v155, v147, s35
	v_lshl_add_u64 v[164:165], v[166:167], 0, v[164:165]
	v_perm_b32 v155, v155, v147, s36
	global_store_dwordx4 v[164:165], v[148:151], off nt
	global_store_dwordx4 v[164:165], v[152:155], off offset:2048 nt
	s_mov_b64 s[0:1], 0
	v_add_co_u32_e32 v148, vcc, 0x1000, v164
	s_nop 1
	v_addc_co_u32_e32 v149, vcc, 0, v165, vcc
	global_store_dwordx4 v[148:149], v[156:159], off nt
	global_store_dwordx4 v[148:149], v[160:163], off offset:2048 nt
	s_waitcnt lgkmcnt(0)
.LBB0_922:
	s_andn2_b64 vcc, exec, s[0:1]
	s_cbranch_vccnz .LBB0_896
	s_cmp_gt_i32 s22, 0x17fff
	s_cbranch_scc1 .Lcvw_b2_drain
	s_waitcnt vmcnt(20)
	s_branch .Lcvw_b2_go

.Lcvw_b2_go:
	v_pk_mul_f32 v[148:149], v[42:43], s[10:11] op_sel_hi:[1,0]
	v_mov_b32_e32 v147, v131
	v_cvt_pk_fp8_f32 v147, v148, v149
	v_pk_mul_f32 v[148:149], v[46:47], s[10:11] op_sel_hi:[1,0]
	v_mov_b32_e32 v150, v131
	v_cvt_pk_fp8_f32 v150, v148, v149
	v_pk_mul_f32 v[148:149], v[44:45], s[10:11] op_sel_hi:[1,0]
	v_mov_b32_e32 v151, v131
	v_cvt_pk_fp8_f32 v147, v148, v149 op_sel:[0,0,1]
	v_pk_mul_f32 v[148:149], v[48:49], s[10:11] op_sel_hi:[1,0]
	v_mov_b32_e32 v152, v131
	v_cvt_pk_fp8_f32 v150, v148, v149 op_sel:[0,0,1]
	v_pk_mul_f32 v[148:149], v[58:59], s[10:11] op_sel_hi:[1,0]
	v_mov_b32_e32 v153, v131
	v_cvt_pk_fp8_f32 v151, v148, v149
	v_pk_mul_f32 v[148:149], v[62:63], s[10:11] op_sel_hi:[1,0]
	v_mov_b32_e32 v154, v131
	v_cvt_pk_fp8_f32 v152, v148, v149
	v_pk_mul_f32 v[148:149], v[60:61], s[10:11] op_sel_hi:[1,0]
	v_mov_b32_e32 v155, v131
	v_cvt_pk_fp8_f32 v151, v148, v149 op_sel:[0,0,1]
	v_pk_mul_f32 v[148:149], v[64:65], s[10:11] op_sel_hi:[1,0]
	v_mov_b32_e32 v156, v131
	v_cvt_pk_fp8_f32 v152, v148, v149 op_sel:[0,0,1]
	v_pk_mul_f32 v[148:149], v[70:71], s[10:11] op_sel_hi:[1,0]
	s_ashr_i32 s0, s42, 31
	v_cvt_pk_fp8_f32 v153, v148, v149
	v_pk_mul_f32 v[148:149], v[78:79], s[10:11] op_sel_hi:[1,0]
	s_lshr_b32 s0, s0, 21
	v_cvt_pk_fp8_f32 v154, v148, v149
	v_pk_mul_f32 v[148:149], v[72:73], s[10:11] op_sel_hi:[1,0]
	s_add_i32 s1, s42, s0
	v_cvt_pk_fp8_f32 v153, v148, v149 op_sel:[0,0,1]
	v_pk_mul_f32 v[148:149], v[80:81], s[10:11] op_sel_hi:[1,0]
	s_ashr_i32 s0, s1, 11
	v_cvt_pk_fp8_f32 v154, v148, v149 op_sel:[0,0,1]
	v_pk_mul_f32 v[148:149], v[82:83], s[10:11] op_sel_hi:[1,0]
	s_and_b32 s1, s1, 0xf800
	v_cvt_pk_fp8_f32 v155, v148, v149
	v_pk_mul_f32 v[148:149], v[90:91], s[10:11] op_sel_hi:[1,0]
	s_sub_i32 s1, s42, s1
	v_cvt_pk_fp8_f32 v156, v148, v149
	v_pk_mul_f32 v[148:149], v[84:85], s[10:11] op_sel_hi:[1,0]
	s_sext_i32_i16 s8, s1
	v_cvt_pk_fp8_f32 v155, v148, v149 op_sel:[0,0,1]
	v_pk_mul_f32 v[148:149], v[92:93], s[10:11] op_sel_hi:[1,0]
	s_bfe_u32 s8, s8, 0x70018
	v_cvt_pk_fp8_f32 v156, v148, v149 op_sel:[0,0,1]
	ds_write2_b32 v136, v147, v150 offset1:72
	ds_write2_b32 v136, v151, v152 offset0:144 offset1:216
	ds_write2_b32 v146, v153, v154 offset0:32 offset1:104
	ds_write2_b32 v146, v155, v156 offset0:176 offset1:248
	v_pk_mul_f32 v[146:147], v[98:99], s[10:11] op_sel_hi:[1,0]
	v_mov_b32_e32 v148, v131
	v_cvt_pk_fp8_f32 v148, v146, v147
	v_pk_mul_f32 v[146:147], v[102:103], s[10:11] op_sel_hi:[1,0]
	v_mov_b32_e32 v149, v131
	v_cvt_pk_fp8_f32 v149, v146, v147
	v_pk_mul_f32 v[146:147], v[100:101], s[10:11] op_sel_hi:[1,0]
	v_mov_b32_e32 v150, v131
	v_cvt_pk_fp8_f32 v148, v146, v147 op_sel:[0,0,1]
	v_pk_mul_f32 v[146:147], v[104:105], s[10:11] op_sel_hi:[1,0]
	v_mov_b32_e32 v151, v131
	v_cvt_pk_fp8_f32 v149, v146, v147 op_sel:[0,0,1]
	v_pk_mul_f32 v[146:147], v[106:107], s[10:11] op_sel_hi:[1,0]
	v_mov_b32_e32 v152, v131
	v_cvt_pk_fp8_f32 v150, v146, v147
	v_pk_mul_f32 v[146:147], v[110:111], s[10:11] op_sel_hi:[1,0]
	v_mov_b32_e32 v153, v131
	v_cvt_pk_fp8_f32 v151, v146, v147
	v_pk_mul_f32 v[146:147], v[108:109], s[10:11] op_sel_hi:[1,0]
	v_mov_b32_e32 v154, v131
	v_cvt_pk_fp8_f32 v150, v146, v147 op_sel:[0,0,1]
	v_pk_mul_f32 v[146:147], v[112:113], s[10:11] op_sel_hi:[1,0]
	v_mov_b32_e32 v155, v131
	v_cvt_pk_fp8_f32 v151, v146, v147 op_sel:[0,0,1]
	v_pk_mul_f32 v[146:147], v[114:115], s[10:11] op_sel_hi:[1,0]
	s_add_i32 s14, s1, s8
	v_cvt_pk_fp8_f32 v152, v146, v147
	v_pk_mul_f32 v[146:147], v[118:119], s[10:11] op_sel_hi:[1,0]
	s_sext_i32_i16 s8, s14
	v_cvt_pk_fp8_f32 v153, v146, v147
	v_pk_mul_f32 v[146:147], v[116:117], s[10:11] op_sel_hi:[1,0]
	s_and_b32 s14, s14, 0xff80
	v_cvt_pk_fp8_f32 v152, v146, v147 op_sel:[0,0,1]
	v_pk_mul_f32 v[146:147], v[120:121], s[10:11] op_sel_hi:[1,0]
	s_sub_i32 s1, s1, s14
	v_cvt_pk_fp8_f32 v153, v146, v147 op_sel:[0,0,1]
	v_pk_mul_f32 v[146:147], v[122:123], s[10:11] op_sel_hi:[1,0]
	s_sext_i32_i16 s14, s1
	v_cvt_pk_fp8_f32 v154, v146, v147
	v_pk_mul_f32 v[146:147], v[126:127], s[10:11] op_sel_hi:[1,0]
	v_lshl_or_b32 v162, s14, 5, v134
	v_cvt_pk_fp8_f32 v155, v146, v147
	v_pk_mul_f32 v[146:147], v[124:125], s[10:11] op_sel_hi:[1,0]
	s_ashr_i32 s1, s0, 31
	v_cvt_pk_fp8_f32 v154, v146, v147 op_sel:[0,0,1]
	v_pk_mul_f32 v[146:147], v[128:129], s[10:11] op_sel_hi:[1,0]
	v_cmp_lt_i32_e32 vcc, s37, v162
	v_cvt_pk_fp8_f32 v155, v146, v147 op_sel:[0,0,1]
	ds_write2_b32 v142, v148, v149 offset0:64 offset1:136
	ds_write2_b32 v143, v150, v151 offset0:80 offset1:152
	ds_write2_b32 v144, v152, v153 offset0:96 offset1:168
	ds_write2_b32 v145, v154, v155 offset0:112 offset1:184
	s_waitcnt lgkmcnt(0)
	ds_read2_b32 v[144:145], v137 offset0:18 offset1:27
	ds_read2_b32 v[142:143], v137 offset1:9
	ds_read2_b32 v[148:149], v137 offset0:54 offset1:63
	ds_read2_b32 v[158:159], v137 offset0:108 offset1:117
	ds_read2_b32 v[160:161], v137 offset0:126 offset1:135
	s_waitcnt lgkmcnt(4)
	v_perm_b32 v147, v145, v144, s33
	v_perm_b32 v151, v145, v144, s34
	ds_read2_b32 v[144:145], v137 offset0:36 offset1:45
	s_waitcnt lgkmcnt(4)
	v_perm_b32 v146, v143, v142, s33
	v_perm_b32 v143, v143, v142, s34
	v_perm_b32 v142, v147, v146, s35
	v_perm_b32 v146, v147, v146, s36
	v_perm_b32 v150, v151, v143, s35
	v_perm_b32 v154, v151, v143, s36
	s_waitcnt lgkmcnt(0)
	v_perm_b32 v147, v145, v144, s33
	v_perm_b32 v152, v145, v144, s34
	v_perm_b32 v151, v149, v148, s33
	v_perm_b32 v153, v149, v148, s34
	ds_read2_b32 v[144:145], v137 offset0:72 offset1:81
	ds_read2_b32 v[148:149], v137 offset0:90 offset1:99
	v_perm_b32 v143, v151, v147, s35
	v_perm_b32 v147, v151, v147, s36
	v_perm_b32 v151, v153, v152, s35
	v_perm_b32 v155, v153, v152, s36
	s_waitcnt lgkmcnt(1)
	v_perm_b32 v152, v145, v144, s33
	v_perm_b32 v145, v145, v144, s34
	s_waitcnt lgkmcnt(0)
	v_perm_b32 v153, v149, v148, s33
	v_perm_b32 v149, v149, v148, s34
	v_perm_b32 v144, v153, v152, s35
	v_perm_b32 v148, v153, v152, s36
	v_perm_b32 v152, v149, v145, s35
	v_perm_b32 v156, v149, v145, s36
	v_perm_b32 v149, v159, v158, s33
	v_perm_b32 v157, v159, v158, s34
	v_perm_b32 v153, v161, v160, s33
	v_perm_b32 v158, v161, v160, s34
	v_add_u32_e32 v160, 0xfffff800, v162
	s_and_b32 s8, s8, 0xffffff80
	s_lshl_b64 s[0:1], s[0:1], 23
	v_cndmask_b32_e32 v160, v162, v160, vcc
	s_add_u32 s0, s16, s0
	v_lshlrev_b32_e32 v161, 1, v160
	s_addc_u32 s1, s17, s1
	s_ashr_i32 s14, s8, 31
	v_and_b32_e32 v161, 0xffffff00, v161
	v_cndmask_b32_e32 v163, 0, v138, vcc
	v_and_b32_e32 v160, 0x7c, v160
	s_add_u32 s0, s0, s8
	v_or3_b32 v160, v160, v163, v161
	s_addc_u32 s1, s1, s14
	v_ashrrev_i32_e32 v161, 31, v160
	v_perm_b32 v145, v153, v149, s35
	v_perm_b32 v149, v153, v149, s36
	v_perm_b32 v153, v158, v157, s35
	v_perm_b32 v157, v158, v157, s36
	v_lshl_add_u64 v[158:159], s[0:1], 0, v[132:133]
	v_lshlrev_b64 v[160:161], 11, v[160:161]
	v_lshl_add_u64 v[160:161], v[158:159], 0, v[160:161]
	v_cmp_lt_i32_e32 vcc, s38, v162
	global_store_dwordx4 v[160:161], v[142:145], off nt
	s_nop 1
	v_cndmask_b32_e32 v142, 1, v139, vcc
	v_add_u32_e32 v142, v142, v162
	v_lshlrev_b32_e32 v143, 1, v142
	v_and_b32_e32 v143, 0xffffff00, v143
	v_cndmask_b32_e32 v144, 0, v138, vcc
	v_and_b32_e32 v142, 0x7d, v142
	v_or3_b32 v142, v142, v144, v143
	v_ashrrev_i32_e32 v143, 31, v142
	v_lshlrev_b64 v[142:143], 11, v[142:143]
	v_lshl_add_u64 v[142:143], v[158:159], 0, v[142:143]
	v_cmp_lt_i32_e32 vcc, s39, v162
	global_store_dwordx4 v[142:143], v[146:149], off nt
	s_nop 0
	v_cndmask_b32_e32 v142, 2, v140, vcc
	v_add_u32_e32 v142, v142, v162
	v_lshlrev_b32_e32 v143, 1, v142
	v_and_b32_e32 v143, 0xffffff00, v143
	v_cndmask_b32_e32 v144, 0, v138, vcc
	v_and_b32_e32 v142, 0x7e, v142
	v_or3_b32 v142, v142, v144, v143
	v_ashrrev_i32_e32 v143, 31, v142
	v_lshlrev_b64 v[142:143], 11, v[142:143]
	v_lshl_add_u64 v[142:143], v[158:159], 0, v[142:143]
	v_cmp_lt_i32_e32 vcc, s40, v162
	global_store_dwordx4 v[142:143], v[150:153], off nt
	s_nop 0
	v_cndmask_b32_e32 v142, 3, v141, vcc
	v_add_u32_e32 v142, v142, v162
	v_lshlrev_b32_e32 v143, 1, v142
	v_and_b32_e32 v143, 0xffffff00, v143
	v_cndmask_b32_e32 v144, 0, v138, vcc
	v_and_b32_e32 v142, 0x7f, v142
	v_or3_b32 v142, v142, v144, v143
	v_ashrrev_i32_e32 v143, 31, v142
	v_lshlrev_b64 v[142:143], 11, v[142:143]
	v_lshl_add_u64 v[142:143], v[158:159], 0, v[142:143]
	global_store_dwordx4 v[142:143], v[154:157], off nt
	s_waitcnt lgkmcnt(0)
	s_branch .LBB0_896

	.amdhsa_kernel _Z3fwd4Args
		.amdhsa_group_segment_fixed_size 0
		.amdhsa_private_segment_fixed_size 0
		.amdhsa_kernarg_size 536
		.amdhsa_user_sgpr_count 2
		.amdhsa_user_sgpr_dispatch_ptr 0
		.amdhsa_user_sgpr_queue_ptr 0
		.amdhsa_user_sgpr_kernarg_segment_ptr 1
		.amdhsa_user_sgpr_dispatch_id 0
		.amdhsa_user_sgpr_kernarg_preload_length 0
		.amdhsa_user_sgpr_kernarg_preload_offset 0
		.amdhsa_user_sgpr_private_segment_size 0
		.amdhsa_uses_dynamic_stack 0
		.amdhsa_enable_private_segment 0
		.amdhsa_system_sgpr_workgroup_id_x 1
		.amdhsa_system_sgpr_workgroup_id_y 0
		.amdhsa_system_sgpr_workgroup_id_z 0
		.amdhsa_system_sgpr_workgroup_info 0
		.amdhsa_system_vgpr_workitem_id 0
		.amdhsa_next_free_vgpr 256
		.amdhsa_next_free_sgpr 102
		.amdhsa_accum_offset 256
		.amdhsa_reserve_vcc 1
		.amdhsa_float_round_mode_32 0
		.amdhsa_float_round_mode_16_64 0
		.amdhsa_float_denorm_mode_32 3
		.amdhsa_float_denorm_mode_16_64 3
		.amdhsa_dx10_clamp 1
		.amdhsa_ieee_mode 1
		.amdhsa_fp16_overflow 0
		.amdhsa_tg_split 0
		.amdhsa_exception_fp_ieee_invalid_op 0
		.amdhsa_exception_fp_denorm_src 0
		.amdhsa_exception_fp_ieee_div_zero 0
		.amdhsa_exception_fp_ieee_overflow 0
		.amdhsa_exception_fp_ieee_underflow 0
		.amdhsa_exception_fp_ieee_inexact 0
		.amdhsa_exception_int_div_zero 0
	.end_amdhsa_kernel

.Lfunc_end0:
	.size	_Z3fwd4Args, .Lfunc_end0-_Z3fwd4Args
	.set _Z3fwd4Args.num_vgpr, 256
	.set _Z3fwd4Args.num_agpr, 0
	.set _Z3fwd4Args.numbered_sgpr, 102
	.set _Z3fwd4Args.num_named_barrier, 0
	.set _Z3fwd4Args.private_seg_size, 0
	.set _Z3fwd4Args.uses_vcc, 1
	.set _Z3fwd4Args.uses_flat_scratch, 0
	.set _Z3fwd4Args.has_dyn_sized_stack, 0
	.set _Z3fwd4Args.has_recursion, 0
	.set _Z3fwd4Args.has_indirect_call, 0

amdhsa.kernels:
  - .agpr_count:     0
    .args:
      - .offset:         0
        .size:           280
        .value_kind:     by_value
      - .offset:         280
        .size:           4
        .value_kind:     hidden_block_count_x
      - .offset:         284
        .size:           4
        .value_kind:     hidden_block_count_y
      - .offset:         288
        .size:           4
        .value_kind:     hidden_block_count_z
      - .offset:         292
        .size:           2
        .value_kind:     hidden_group_size_x
      - .offset:         294
        .size:           2
        .value_kind:     hidden_group_size_y
      - .offset:         296
        .size:           2
        .value_kind:     hidden_group_size_z
      - .offset:         298
        .size:           2
        .value_kind:     hidden_remainder_x
      - .offset:         300
        .size:           2
        .value_kind:     hidden_remainder_y
      - .offset:         302
        .size:           2
        .value_kind:     hidden_remainder_z
      - .offset:         320
        .size:           8
        .value_kind:     hidden_global_offset_x
      - .offset:         328
        .size:           8
        .value_kind:     hidden_global_offset_y
      - .offset:         336
        .size:           8
        .value_kind:     hidden_global_offset_z
      - .offset:         344
        .size:           2
        .value_kind:     hidden_grid_dims
      - .offset:         400
        .size:           4
        .value_kind:     hidden_dynamic_lds_size
    .group_segment_fixed_size: 0
    .kernarg_segment_align: 8
    .kernarg_segment_size: 536
    .language:       OpenCL C
    .language_version:
      - 2
      - 0
    .max_flat_workgroup_size: 512
    .name:           _Z3fwd4Args
    .private_segment_fixed_size: 0
    .sgpr_count:     108
    .sgpr_spill_count: 80
    .symbol:         _Z3fwd4Args.kd
    .uniform_work_group_size: 1
    .uses_dynamic_stack: false
    .vgpr_count:     256
    .vgpr_spill_count: 0
    .wavefront_size: 64
